# speedup vs baseline: 1.0075x; 1.0006x over previous
_Z11prep_kernelPKfS0_S0_S0_PDF16_S1_S0_S1_:
	s_getpc_b64 s[24:25]
	v_lshlrev_b32_e32 v172, 7, v0
	v_min_u32_e32 v172, 0x5800, v172
	global_load_dword v173, v172, s[24:25]
	s_load_dwordx8 s[4:11], s[0:1], 0x0
	s_load_dwordx4 s[12:15], s[0:1], 0x20
	s_mov_b32 s3, 0
	s_lshl_b64 s[2:3], s[2:3], 6
	v_cmp_gt_u32_e32 vcc, 8, v0
	v_lshlrev_b32_e32 v1, 3, v0
	s_and_saveexec_b64 s[16:17], vcc
	s_cbranch_execz .LBB0_2
	s_load_dwordx4 s[20:23], s[0:1], 0x30
	v_or_b32_e32 v10, s2, v1
	v_mov_b32_e32 v11, s3
	s_waitcnt lgkmcnt(0)
	v_lshl_add_u64 v[12:13], v[10:11], 2, s[20:21]
	global_load_dwordx4 v[2:5], v[12:13], off
	global_load_dwordx4 v[6:9], v[12:13], off offset:16
	s_waitcnt vmcnt(1)
	v_cvt_pk_f16_f32 v2, v2, v3
	v_cvt_pk_f16_f32 v3, v4, v5
	s_waitcnt vmcnt(0)
	v_cvt_pk_f16_f32 v4, v6, v7
	v_lshl_add_u64 v[6:7], v[10:11], 1, s[22:23]
	v_cvt_pk_f16_f32 v5, v8, v9
	global_store_dwordx4 v[6:7], v[2:5], off

_Z11attn_kernelPKDF16_S0_PDF16_P15HIP_vector_typeIfLj2EE:
	s_getpc_b64 s[38:39]
	v_lshlrev_b32_e32 v240, 7, v0
	v_min_u32_e32 v240, 0x3380, v240
	global_load_dword v241, v240, s[38:39]
	s_mov_b32 s5, 0
	s_mov_b32 s28, s3
	s_load_dwordx8 s[20:27], s[0:1], 0x0
	s_mov_b32 s3, s5
	s_lshl_b64 s[0:1], s[4:5], 12
	s_lshl_b64 s[2:3], s[2:3], 8
	s_add_u32 s0, s0, s2
	v_lshrrev_b32_e32 v1, 6, v0
	s_addc_u32 s1, s1, s3
	v_and_b32_e32 v160, 31, v0
	s_lshl_b64 s[2:3], s[0:1], 8
	v_lshlrev_b32_e32 v162, 5, v1
	s_waitcnt lgkmcnt(0)
	s_add_u32 s2, s20, s2
	v_or_b32_e32 v2, v162, v160
	v_bfe_u32 v54, v0, 5, 1
	s_addc_u32 s3, s21, s3
	v_lshlrev_b32_e32 v164, 8, v2
	v_mov_b32_e32 v165, 0
	v_lshl_add_u64 v[2:3], s[2:3], 0, v[164:165]
	v_lshlrev_b32_e32 v164, 4, v54
	v_lshl_add_u64 v[2:3], v[2:3], 0, v[164:165]
	global_load_dwordx4 v[156:159], v[2:3], off
	global_load_dwordx4 v[152:155], v[2:3], off offset:32
	global_load_dwordx4 v[148:151], v[2:3], off offset:64
	global_load_dwordx4 v[144:147], v[2:3], off offset:96
	global_load_dwordx4 v[140:143], v[2:3], off offset:128
	global_load_dwordx4 v[136:139], v[2:3], off offset:160
	global_load_dwordx4 v[132:135], v[2:3], off offset:192
	global_load_dwordx4 v[128:131], v[2:3], off offset:224
	s_ashr_i32 s29, s28, 31
	v_bfe_u32 v55, v0, 2, 3
	s_lshl_b64 s[2:3], s[4:5], 20
	s_lshl_b64 s[20:21], s[28:29], 18
	v_lshl_or_b32 v2, v1, 3, v55
	s_add_u32 s4, s22, s2
	v_lshrrev_b32_e32 v3, 2, v2
	s_addc_u32 s7, s23, s3
	v_xor_b32_e32 v4, v3, v0
	s_add_u32 s6, s4, s20
	v_and_b32_e32 v5, 32, v0
	v_lshlrev_b32_e32 v4, 3, v4
	v_lshlrev_b32_e32 v1, 11, v1
	s_addc_u32 s7, s7, s21
	v_lshlrev_b32_e32 v164, 8, v2
	v_and_or_b32 v4, v4, 24, v5
	v_add_u32_e32 v173, 0, v1
	v_lshl_add_u64 v[2:3], s[6:7], 0, v[164:165]
	v_lshlrev_b32_e32 v164, 1, v4
	v_readfirstlane_b32 s4, v173
	v_add_u32_e32 v6, 0x400, v173
	v_lshl_add_u64 v[2:3], v[2:3], 0, v[164:165]
	s_mov_b64 s[6:7], 0x80
	s_mov_b32 m0, s4
	v_readfirstlane_b32 s4, v6
	v_add_u32_e32 v6, 0x4000, v173
	v_lshl_add_u64 v[4:5], v[2:3], 0, s[6:7]
	global_load_lds_dwordx4 v[2:3], off
	s_mov_b32 m0, s4
	s_mov_b64 s[6:7], 0x4000
	v_readfirstlane_b32 s4, v6
	global_load_lds_dwordx4 v[4:5], off
	v_lshl_add_u64 v[4:5], v[2:3], 0, s[6:7]
	s_mov_b32 m0, s4
	s_mov_b64 s[6:7], 0x4080
	global_load_lds_dwordx4 v[4:5], off
	v_add_u32_e32 v4, 0x4400, v173
	v_lshl_add_u64 v[2:3], v[2:3], 0, s[6:7]
	v_readfirstlane_b32 s4, v4
	s_mov_b32 m0, s4
	s_movk_i32 s4, 0x1c0
	global_load_lds_dwordx4 v[2:3], off
	v_lshlrev_b32_e32 v2, 8, v0
	v_and_b32_e32 v2, 0x1800, v2
	v_lshlrev_b32_e32 v3, 6, v0
	v_and_or_b32 v6, v3, s4, v2
	v_xor_b32_e32 v2, v54, v55
	v_lshlrev_b32_e32 v2, 4, v2
	v_and_or_b32 v175, v2, 48, v6
	s_waitcnt vmcnt(2)
	v_add_u32_e32 v172, 0, v175
	s_waitcnt lgkmcnt(0)
	s_barrier
	ds_read_b128 v[2:5], v172
	ds_read_b128 v[34:37], v172 offset:512
	v_bitop3_b32 v7, v54, v55, 2 bitop3:0x36
	v_lshlrev_b32_e32 v7, 4, v7
	v_and_or_b32 v176, v7, 48, v6
	v_add_u32_e32 v174, 0, v176
	ds_read_b128 v[18:21], v174
	ds_read_b128 v[38:41], v174 offset:512
	s_mov_b32 s33, 0x41200000
	s_cmp_lg_u32 0, -1
	s_cselect_b32 s37, 0, 0
	s_waitcnt vmcnt(0) lgkmcnt(0)
	v_mfma_f32_32x32x16_f16 v[2:17], v[2:5], v[156:159], 0
	s_movk_i32 s4, 0x110
	v_and_b32_e32 v161, 63, v0
	v_lshl_or_b32 v1, v55, 8, v1
	s_mov_b32 s18, s5
	s_mov_b32 s19, s5
	s_mov_b32 s6, s5
	s_mov_b32 s7, s5
	v_mfma_f32_32x32x16_f16 v[2:17], v[18:21], v[152:155], v[2:17]
	ds_read_b128 v[18:21], v172 offset:8192
	ds_read_b128 v[42:45], v172 offset:8704
	ds_read_b128 v[46:49], v174 offset:8192
	ds_read_b128 v[50:53], v174 offset:8704
	s_mov_b32 s8, s5
	s_mov_b32 s9, s5
	s_mov_b32 s10, s5
	s_mov_b32 s11, s5
	s_mov_b32 s12, s5
	s_waitcnt lgkmcnt(3)
	v_mfma_f32_32x32x16_f16 v[18:33], v[18:21], v[156:159], 0
	s_mov_b32 s13, s5
	s_mov_b32 s14, s5
	s_mov_b32 s15, s5
	s_mov_b32 s16, s5
	s_mov_b32 s17, s5
	s_mov_b32 s36, 1
	s_mov_b32 s34, -1
	s_waitcnt lgkmcnt(1)
	v_mfma_f32_32x32x16_f16 v[18:33], v[46:49], v[152:155], v[18:33]
	s_mov_b32 s35, 2
	s_mov_b64 s[30:31], 0x8000
	v_mfma_f32_32x32x16_f16 v[2:17], v[34:37], v[148:151], v[2:17]
	v_mfma_f32_32x32x16_f16 v[18:33], v[42:45], v[148:151], v[18:33]
	v_mfma_f32_32x32x16_f16 v[2:17], v[38:41], v[144:147], v[2:17]
	ds_read_b128 v[34:37], v172 offset:1024
	ds_read_b128 v[38:41], v172 offset:1536
	s_waitcnt lgkmcnt(2)
	v_mfma_f32_32x32x16_f16 v[18:33], v[50:53], v[144:147], v[18:33]
	s_waitcnt lgkmcnt(1)
	v_mfma_f32_32x32x16_f16 v[2:17], v[34:37], v[140:143], v[2:17]
	ds_read_b128 v[34:37], v172 offset:9216
	ds_read_b128 v[42:45], v172 offset:9728
	s_waitcnt lgkmcnt(1)
	v_mfma_f32_32x32x16_f16 v[18:33], v[34:37], v[140:143], v[18:33]
	ds_read_b128 v[34:37], v174 offset:1024
	ds_read_b128 v[46:49], v174 offset:1536
	s_waitcnt lgkmcnt(1)
	v_mfma_f32_32x32x16_f16 v[2:17], v[34:37], v[136:139], v[2:17]
	ds_read_b128 v[34:37], v174 offset:9216
	ds_read_b128 v[50:53], v174 offset:9728
	v_mfma_f32_32x32x16_f16 v[2:17], v[38:41], v[132:135], v[2:17]
	s_waitcnt lgkmcnt(1)
	v_mfma_f32_32x32x16_f16 v[18:33], v[34:37], v[136:139], v[18:33]
	v_mov_b32_e32 v34, 0xf149f2ca
	v_mfma_f32_32x32x16_f16 v[2:17], v[46:49], v[128:131], v[2:17]
	v_mfma_f32_32x32x16_f16 v[18:33], v[42:45], v[132:135], v[18:33]
	s_nop 10
	v_max_f32_e32 v35, v3, v3
	v_max_f32_e32 v36, v2, v2
	v_max_f32_e32 v35, v36, v35
	v_max3_f32 v35, v35, v4, v5
	v_max3_f32 v35, v35, v6, v7
	v_max3_f32 v35, v35, v8, v9
	v_max3_f32 v35, v35, v10, v11
	s_waitcnt lgkmcnt(0)
	v_mfma_f32_32x32x16_f16 v[18:33], v[50:53], v[128:131], v[18:33]
	v_max3_f32 v35, v35, v12, v13
	v_max3_f32 v35, v35, v14, v15
	v_max3_f32 v35, v35, v16, v17
	s_nop 8
	v_max3_f32 v35, v35, v18, v19
	v_max3_f32 v35, v35, v20, v21
	v_max3_f32 v35, v35, v22, v23
	v_max3_f32 v35, v35, v24, v25
	v_max3_f32 v35, v35, v26, v27
	v_max3_f32 v35, v35, v28, v29
	v_max3_f32 v35, v35, v30, v31
	v_max3_f32 v35, v35, v32, v33
	v_mov_b32_e32 v36, v35
	s_nop 1
	v_permlane32_swap_b32_e32 v35, v36
	v_max_f32_e32 v36, v36, v36
	v_max_f32_e32 v35, v35, v35
	v_max_f32_e32 v35, v35, v36
	v_add_f32_e32 v36, 0x7149f2ca, v35
	v_cmp_ge_f32_e32 vcc, s33, v36
	s_cmp_eq_u64 vcc, exec
	v_max_f32_e32 v35, 0xf149f2ca, v35
	s_cselect_b64 vcc, -1, 0
	v_cndmask_b32_e32 v168, v35, v34, vcc
	v_sub_f32_e32 v96, v18, v168
	v_sub_f32_e32 v97, v19, v168
	v_lshlrev_b32_e32 v18, 4, v0
	v_lshrrev_b32_e32 v19, 4, v0
	v_sub_f32_e32 v98, v20, v168
	v_and_b32_e32 v18, 0xc0, v18
	v_bitop3_b32 v19, v19, v54, 1 bitop3:0x6c
	v_lshlrev_b32_e32 v20, 3, v0
	v_sub_f32_e32 v99, v21, v168
	v_lshl_or_b32 v18, v54, 11, v18
	v_lshlrev_b32_e32 v19, 5, v19
	v_and_b32_e32 v21, 8, v20
	v_or3_b32 v18, v18, v21, v19
	v_and_b32_e32 v19, 16, v20
	v_sub_f32_e32 v0, 0xf149f2ca, v35
	v_add3_u32 v163, v19, s37, v18
	v_bitop3_b32 v169, v18, s4, v19 bitop3:0x36
	v_exp_f32_e32 v18, v0
	s_add_u32 s2, s2, s20
	v_sub_f32_e32 v2, v2, v168
	v_sub_f32_e32 v3, v3, v168
	v_sub_f32_e32 v4, v4, v168
	v_sub_f32_e32 v5, v5, v168
	v_sub_f32_e32 v6, v6, v168
	v_sub_f32_e32 v7, v7, v168
	v_sub_f32_e32 v8, v8, v168
	v_sub_f32_e32 v9, v9, v168
	v_sub_f32_e32 v10, v10, v168
	v_sub_f32_e32 v11, v11, v168
	v_sub_f32_e32 v12, v12, v168
	v_sub_f32_e32 v13, v13, v168
	v_sub_f32_e32 v14, v14, v168
	v_sub_f32_e32 v15, v15, v168
	v_sub_f32_e32 v16, v16, v168
	v_sub_f32_e32 v17, v17, v168
	s_addc_u32 s3, s3, s21
	s_mov_b32 s4, s5
	v_exp_f32_e32 v127, v2
	v_exp_f32_e32 v180, v3
	v_exp_f32_e32 v125, v4
	v_exp_f32_e32 v179, v5
	v_exp_f32_e32 v123, v6
	v_exp_f32_e32 v126, v7
	v_exp_f32_e32 v122, v8
	v_exp_f32_e32 v124, v9
	v_exp_f32_e32 v119, v10
	v_exp_f32_e32 v121, v11
	v_exp_f32_e32 v117, v12
	v_exp_f32_e32 v120, v13
	v_exp_f32_e32 v115, v14
	v_exp_f32_e32 v118, v15
	v_exp_f32_e32 v114, v16
	v_exp_f32_e32 v116, v17
	v_or3_b32 v0, s2, v1, v164
	v_mov_b32_e32 v1, s3
	v_lshlrev_b32_e32 v164, 3, v54
	v_mov_b64_e32 v[62:63], s[18:19]
	v_lshl_add_u64 v[0:1], s[22:23], 0, v[0:1]
	s_mov_b64 s[2:3], 0xc080
	v_mov_b64_e32 v[48:49], s[4:5]
	v_sub_f32_e32 v100, v22, v168
	v_sub_f32_e32 v101, v23, v168
	v_sub_f32_e32 v102, v24, v168
	v_sub_f32_e32 v103, v25, v168
	v_sub_f32_e32 v104, v26, v168
	v_sub_f32_e32 v105, v27, v168
	v_sub_f32_e32 v106, v28, v168
	v_sub_f32_e32 v107, v29, v168
	v_sub_f32_e32 v108, v30, v168
	v_sub_f32_e32 v109, v31, v168
	v_sub_f32_e32 v110, v32, v168
	v_sub_f32_e32 v111, v33, v168
	v_lshl_add_u64 v[170:171], v[0:1], 0, s[2:3]
	s_movk_i32 s2, 0xbf80
	s_movk_i32 s20, 0xc000
	s_movk_i32 s22, 0xff80
	v_cndmask_b32_e64 v166, v18, 1.0, vcc
	v_mov_b64_e32 v[60:61], s[16:17]
	v_mov_b64_e32 v[58:59], s[14:15]
	v_mov_b64_e32 v[56:57], s[12:13]
	v_mov_b64_e32 v[54:55], s[10:11]
	v_mov_b64_e32 v[52:53], s[8:9]
	v_mov_b64_e32 v[50:51], s[6:7]
	v_mov_b64_e32 v[32:33], v[48:49]
	v_mov_b64_e32 v[16:17], v[48:49]
	v_mov_b64_e32 v[0:1], v[48:49]
	s_mov_b32 s3, -1
	s_mov_b32 s21, -1
	s_mov_b32 s23, -1
	v_add_u32_e32 v167, s37, v169
	v_mov_b64_e32 v[34:35], v[50:51]
	v_mov_b64_e32 v[36:37], v[52:53]
	v_mov_b64_e32 v[38:39], v[54:55]
	v_mov_b64_e32 v[40:41], v[56:57]
	v_mov_b64_e32 v[42:43], v[58:59]
	v_mov_b64_e32 v[44:45], v[60:61]
	v_mov_b64_e32 v[46:47], v[62:63]
	v_mov_b64_e32 v[18:19], v[50:51]
	v_mov_b64_e32 v[20:21], v[52:53]
	v_mov_b64_e32 v[22:23], v[54:55]
	v_mov_b64_e32 v[24:25], v[56:57]
	v_mov_b64_e32 v[26:27], v[58:59]
	v_mov_b64_e32 v[28:29], v[60:61]
	v_mov_b64_e32 v[30:31], v[62:63]
	v_mov_b64_e32 v[2:3], v[50:51]
	v_mov_b64_e32 v[4:5], v[52:53]
	v_mov_b64_e32 v[6:7], v[54:55]
	v_mov_b64_e32 v[8:9], v[56:57]
	v_mov_b64_e32 v[10:11], v[58:59]
	v_mov_b64_e32 v[12:13], v[60:61]
	v_mov_b64_e32 v[14:15], v[62:63]
